# all remaining per-block loop control (block counter, block range tests, exit) moved to SALU; exec-mask bookkeeping blocks removed
# baseline (speedup 1.0000x reference)
.Lstag_done:
	s_lshl_b32 s84, s95, 3
	s_add_u32 s85, s84, 8
	v_lshlrev_b32_e32 v3, 2, v22
	s_waitcnt vmcnt(0)
	v_mov_b32_e32 v18, v108
	v_mov_b32_e32 v19, v109
	v_mov_b32_e32 v20, v110
	v_mov_b32_e32 v16, v111
	v_mov_b32_e32 v17, v112
	v_mov_b32_e32 v12, v113
	v_mov_b32_e32 v13, v114
	v_mov_b32_e32 v15, v115
	v_mov_b32_e32 v4, 0x180
	v_lshl_or_b32 v23, v8, 2, v4
	v_mov_b32_e32 v21, v116
	v_mov_b32_e32 v4, v117
	v_mov_b32_e32 v5, v118
	v_mov_b32_e32 v10, v119
	v_mov_b32_e32 v3, 0x12810
	v_lshl_add_u32 v23, v9, 10, v3
	ds_read2_b32 v[24:25], v23 offset1:32
	v_add_u32_e32 v2, v23, v2
	ds_read2_b32 v[230:231], v2 offset1:1
	v_lshlrev_b32_e32 v26, 8, v9
	s_lshl_b32 s2, s2, 11
	v_or3_b32 v235, v26, s2, v1
	s_mov_b32 s12, 0x7a120
	s_waitcnt lgkmcnt(1)
	v_readfirstlane_b32 s13, v24
	v_readfirstlane_b32 s6, v25
	v_cmp_gt_i32_e32 vcc, s12, v235
	v_mov_b32_e32 v2, 0
	v_mov_b32_e32 v238, 0
	s_and_saveexec_b64 s[2:3], vcc
	s_cbranch_execz .LBB1_143
	v_ashrrev_i32_e32 v25, 31, v235
	v_mov_b32_e32 v24, v235
	v_lshl_add_u64 v[24:25], v[24:25], 2, s[50:51]
	global_load_dword v238, v[24:25], off
.LBB1_143:
	s_or_b64 exec, exec, s[2:3]
	v_cndmask_b32_e64 v24, v14, 0, s[4:5]
	v_ashrrev_i32_e32 v25, 31, v24
	v_lshlrev_b64 v[24:25], 3, v[24:25]
	s_mov_b64 s[2:3], src_shared_base
	v_lshl_add_u64 v[24:25], s[56:57], 0, v[24:25]
	v_mov_b32_e32 v14, s3
	v_cndmask_b32_e64 v232, v24, 0, s[4:5]
	v_add_lshl_u32 v24, s13, v1, 1
	v_cndmask_b32_e64 v233, v25, v14, s[4:5]
	s_mov_b32 s81, s4
	v_ashrrev_i32_e32 v25, 31, v24
	v_lshl_add_u64 v[24:25], v[24:25], 2, v[232:233]
	flat_load_dwordx2 v[82:83], v[24:25]
	s_mov_b32 s2, 0x4038aa3b
	v_add_f32_e32 v239, s33, v11
	s_waitcnt vmcnt(0)
	v_fma_mixlo_f16 v11, v18, s2, 0
	v_fma_mixlo_f16 v25, v16, s2, 0
	v_fma_mixlo_f16 v27, v17, s2, 0
	v_add_lshl_u32 v22, s13, v22, 1
	v_fma_mixlo_f16 v14, v19, s2, 0
	v_fma_mixlo_f16 v18, v18, s2, -v11 op_sel_hi:[0,0,1]
	v_fma_mixlo_f16 v16, v16, s2, -v25 op_sel_hi:[0,0,1]
	v_fma_mixlo_f16 v17, v17, s2, -v27 op_sel_hi:[0,0,1]
	s_mov_b32 s14, 0x186a0
	v_ashrrev_i32_e32 v23, 31, v22
	v_fma_mixlo_f16 v19, v19, s2, -v14 op_sel_hi:[0,0,1]
	v_cndmask_b32_e64 v11, 0, v11, s[0:1]
	v_cndmask_b32_e64 v14, 0, v14, s[0:1]
	v_cndmask_b32_e64 v25, 0, v25, s[0:1]
	v_cndmask_b32_e64 v27, 0, v27, s[0:1]
	v_cndmask_b32_e64 v18, 0, v18, s[0:1]
	v_cndmask_b32_e64 v16, 0, v16, s[0:1]
	v_cndmask_b32_e64 v17, 0, v17, s[0:1]
	v_pack_b32_f16 v179, v11, v14
	v_pack_b32_f16 v178, v11, v18
	v_pack_b32_f16 v185, v27, v17
	v_pack_b32_f16 v182, v25, v16
	v_lshl_add_u64 v[16:17], v[22:23], 2, v[232:233]
	flat_load_dwordx2 v[236:237], v[16:17]
	v_mov_b32_e32 v17, v2
	v_cndmask_b32_e64 v19, 0, v19, s[0:1]
	v_pack_b32_f16 v180, v19, v14
	v_fma_mixlo_f16 v14, v13, s2, 0
	v_fma_mixlo_f16 v13, v13, s2, -v14 op_sel_hi:[0,0,1]
	v_cndmask_b32_e64 v14, 0, v14, s[0:1]
	v_cndmask_b32_e64 v13, 0, v13, s[0:1]
	v_fma_mixlo_f16 v24, v20, s2, 0
	v_fma_mixlo_f16 v26, v21, s2, 0
	v_or_b32_e32 v240, 64, v1
	v_pack_b32_f16 v188, v13, v14
	v_fma_mixlo_f16 v13, v10, s2, 0
	v_lshl_add_u32 v244, v1, 2, v3
	v_and_b32_e32 v0, 32, v0
	v_mov_b32_e32 v1, 0xa300
	v_fma_mixlo_f16 v20, v20, s2, -v24 op_sel_hi:[0,0,1]
	v_fma_mixlo_f16 v21, v21, s2, -v26 op_sel_hi:[0,0,1]
	v_fma_mixlo_f16 v10, v10, s2, -v13 op_sel_hi:[0,0,1]
	v_lshl_or_b32 v245, v0, 2, v1
	v_lshl_add_u32 v246, v8, 4, v1
	v_add_u32_e32 v3, 64, v7
	v_cndmask_b32_e64 v24, 0, v24, s[0:1]
	v_cndmask_b32_e64 v26, 0, v26, s[0:1]
	v_cndmask_b32_e64 v20, 0, v20, s[0:1]
	v_cndmask_b32_e64 v21, 0, v21, s[0:1]
	v_cndmask_b32_e64 v13, 0, v13, s[0:1]
	v_cndmask_b32_e64 v10, 0, v10, s[0:1]
	v_mov_b32_e32 v0, 0xc0
	v_pack_b32_f16 v183, v25, v26
	v_pack_b32_f16 v181, v24, v20
	v_pack_b32_f16 v184, v21, v26
	v_pack_b32_f16 v193, v13, v10
	v_lshlrev_b32_e32 v251, 3, v9
	v_mov_b32_e32 v7, v2
	v_mov_b32_e32 v9, v2
	v_mov_b32_e32 v10, v2
	v_mov_b32_e32 v13, v2
	v_add_u32_e32 v242, 8, v251
	s_waitcnt lgkmcnt(0)
	v_sub_u32_e32 v234, v231, v230
	s_mov_b64 s[4:5], 0
	v_mov_b32_e32 v249, s6
	s_mov_b32 s71, s6
	v_mov_b32_e32 v231, s13
	s_mov_b32 s70, s13
	s_mov_b32 s15, 0x5040100
	s_mov_b32 s82, 1.0
	s_mov_b32 s83, 1.0
	s_mov_b32 s73, 0x3c000000
	s_mov_b32 s74, 0x42004000
	s_mov_b32 s75, 0x48804800
	s_mov_b32 s76, 0x49804900
	s_mov_b32 s77, 0x4c404c00
	s_mov_b32 s78, 0x4cc04c80
	s_mov_b32 s79, 0x4e404e00
	s_mov_b32 s80, 0x4ec04e80
	v_mov_b32_e32 v197, 0x3c003c00
	s_mov_b32 s16, 0x10000
	s_mov_b32 s17, 0x7a100
	v_lshl_or_b32 v11, v82, 3, 3
	v_cmp_gt_u32_e32 vcc, s14, v82
	v_mov_b32_e32 v196, v83
	s_nop 0
	v_cndmask_b32_e32 v16, 3, v11, vcc
	v_lshl_add_u64 v[16:17], v[16:17], 2, s[54:55]
	global_load_dword v241, v[16:17], off
	v_fma_mixlo_f16 v11, v12, s2, 0
	v_fma_mixlo_f16 v12, v12, s2, -v11 op_sel_hi:[0,0,1]
	v_cndmask_b32_e64 v11, 0, v11, s[0:1]
	v_cndmask_b32_e64 v12, 0, v12, s[0:1]
	v_pack_b32_f16 v187, v11, v14
	v_pack_b32_f16 v186, v11, v12
	v_fma_mixlo_f16 v11, v4, s2, 0
	v_fma_mixlo_f16 v4, v4, s2, -v11 op_sel_hi:[0,0,1]
	v_cndmask_b32_e64 v11, 0, v11, s[0:1]
	v_cndmask_b32_e64 v4, 0, v4, s[0:1]
	v_fma_mixlo_f16 v16, v15, s2, 0
	v_pack_b32_f16 v190, v11, v4
	v_lshrrev_b32_e32 v4, 3, v8
	v_fma_mixlo_f16 v15, v15, s2, -v16 op_sel_hi:[0,0,1]
	v_fma_mixlo_f16 v12, v5, s2, 0
	v_and_b32_e32 v243, 4, v4
	v_cndmask_b32_e64 v16, 0, v16, s[0:1]
	v_cndmask_b32_e64 v15, 0, v15, s[0:1]
	v_fma_mixlo_f16 v5, v5, s2, -v12 op_sel_hi:[0,0,1]
	v_lshl_add_u32 v247, v243, 6, v1
	v_xor_b32_e32 v1, 32, v6
	v_pack_b32_f16 v189, v16, v15
	v_cndmask_b32_e64 v12, 0, v12, s[0:1]
	v_cndmask_b32_e64 v5, 0, v5, s[0:1]
	v_cmp_lt_i32_e32 vcc, v1, v3
	v_mov_b32_e32 v16, v2
	v_mov_b32_e32 v17, v2
	v_pack_b32_f16 v191, v11, v12
	v_pack_b32_f16 v192, v5, v12
	v_lshl_or_b32 v0, v4, 6, v0
	v_cndmask_b32_e32 v1, v6, v1, vcc
	v_mov_b32_e32 v3, v2
	v_mov_b32_e32 v4, v2
	v_mov_b32_e32 v5, v2
	v_mov_b32_e32 v6, v2
	v_mov_b32_e32 v8, v2
	v_mov_b32_e32 v11, v2
	v_mov_b32_e32 v12, v2
	v_mov_b32_e32 v14, v2
	v_mov_b32_e32 v15, v2
	v_mov_b64_e32 v[32:33], v[16:17]
	v_mov_b64_e32 v[48:49], v[16:17]
	v_mov_b64_e32 v[64:65], v[16:17]
	v_mov_b64_e32 v[80:81], v[16:17]
	v_lshlrev_b32_e32 v248, 2, v1
	v_add_u32_e32 v250, 0xa300, v0
	v_mov_b64_e32 v[30:31], v[14:15]
	v_mov_b64_e32 v[28:29], v[12:13]
	v_mov_b64_e32 v[26:27], v[10:11]
	v_mov_b64_e32 v[24:25], v[8:9]
	v_mov_b64_e32 v[22:23], v[6:7]
	v_mov_b64_e32 v[20:21], v[4:5]
	v_mov_b64_e32 v[18:19], v[2:3]
	v_mov_b64_e32 v[46:47], v[14:15]
	v_mov_b64_e32 v[44:45], v[12:13]
	v_mov_b64_e32 v[42:43], v[10:11]
	v_mov_b64_e32 v[40:41], v[8:9]
	v_mov_b64_e32 v[38:39], v[6:7]
	v_mov_b64_e32 v[36:37], v[4:5]
	v_mov_b64_e32 v[34:35], v[2:3]
	v_mov_b64_e32 v[62:63], v[14:15]
	v_mov_b64_e32 v[60:61], v[12:13]
	v_mov_b64_e32 v[58:59], v[10:11]
	v_mov_b64_e32 v[56:57], v[8:9]
	v_mov_b64_e32 v[54:55], v[6:7]
	v_mov_b64_e32 v[52:53], v[4:5]
	v_mov_b64_e32 v[50:51], v[2:3]
	v_mov_b64_e32 v[78:79], v[14:15]
	v_mov_b64_e32 v[76:77], v[12:13]
	v_mov_b64_e32 v[74:75], v[10:11]
	v_mov_b64_e32 v[72:73], v[8:9]
	v_mov_b64_e32 v[70:71], v[6:7]
	v_mov_b64_e32 v[68:69], v[4:5]
	v_mov_b64_e32 v[66:67], v[2:3]
	s_branch .LBB1_145

.Lstep_next:
	v_mov_b32_e32 v196, v237
	s_waitcnt vmcnt(0) lgkmcnt(0)
	v_mov_b64_e32 v[236:237], v[0:1]
	s_mov_b32 s13, s18
	s_branch .LBB1_145

.LBB1_146:
	s_or_b64 exec, exec, s[10:11]
	v_mov_b64_e32 v[234:235], v[16:17]
	v_mov_b32_e32 v251, v82
	s_mov_b32 s70, s71
	s_mov_b32 s71, s20
	s_branch .LBB1_149

.LBB1_151:
	s_cmp_le_i32 s18, s70
	s_cbranch_scc1 .LBB1_153
	s_cmp_ge_i32 s19, s71
	s_cbranch_scc1 .LBB1_153
	v_pk_add_f16 v3, v14, s77 neg_lo:[0,1] neg_hi:[0,1]
	v_pk_add_f16 v4, s77, v15 neg_lo:[0,1] neg_hi:[0,1]
	v_pk_min_f16 v6, v3, v4 clamp
	v_pk_add_f16 v5, v14, s78 neg_lo:[0,1] neg_hi:[0,1]
	v_pk_add_f16 v16, s78, v15 neg_lo:[0,1] neg_hi:[0,1]
	v_pk_min_f16 v7, v5, v16 clamp
	v_pk_add_f16 v3, v14, s79 neg_lo:[0,1] neg_hi:[0,1]
	v_pk_add_f16 v4, s79, v15 neg_lo:[0,1] neg_hi:[0,1]
	v_pk_min_f16 v8, v3, v4 clamp
	v_pk_add_f16 v5, v14, s80 neg_lo:[0,1] neg_hi:[0,1]
	v_pk_add_f16 v16, s80, v15 neg_lo:[0,1] neg_hi:[0,1]
	v_pk_min_f16 v9, v5, v16 clamp
	s_nop 1
	v_mfma_f32_32x32x16_f16 v[66:81], v[202:205], v[6:9], v[66:81]
	v_mfma_f32_32x32x16_f16 v[50:65], v[210:213], v[6:9], v[50:65]
	v_mfma_f32_32x32x16_f16 v[34:49], v[218:221], v[6:9], v[34:49]
	v_mfma_f32_32x32x16_f16 v[18:33], v[226:229], v[6:9], v[18:33]
.LBB1_153:
	s_cmp_ge_i32 s18, s71
	s_cbranch_scc0 .Lstep_next
.Lflush:
	s_setprio 3
	v_cmp_gt_i32_e32 vcc, s12, v235
	s_and_b64 s[10:11], s[0:1], vcc
	v_add_u32_e32 v3, 1, v251
	v_lshl_add_u32 v3, v3, 7, v244
	ds_read2_b32 v[230:231], v3 offset1:1
	ds_read_b128 v[82:85], v245 offset:32768
	ds_read_b128 v[86:89], v245 offset:32784
	ds_read_b128 v[90:93], v245 offset:32800
	ds_read_b128 v[94:97], v245 offset:32816
	ds_read_b128 v[98:101], v245 offset:32832
	ds_read_b128 v[102:105], v245 offset:32848
	ds_read_b128 v[106:109], v245 offset:32864
	ds_read_b128 v[110:113], v245 offset:32880
	ds_read_b128 v[114:117], v246 offset:0
	ds_read_b128 v[118:121], v246 offset:8192
	ds_read_b128 v[122:125], v246 offset:1024
	ds_read_b128 v[126:129], v246 offset:9216
	v_cvt_f32_i32_e32 v16, v234
	v_cvt_pk_f16_f32 v4, v66, v67
	v_cvt_pk_f16_f32 v5, v68, v69
	v_cvt_pk_f16_f32 v6, v70, v71
	v_cvt_pk_f16_f32 v7, v72, v73
	v_cvt_pk_f16_f32 v8, v74, v75
	v_cvt_pk_f16_f32 v9, v76, v77
	v_cvt_pk_f16_f32 v10, v78, v79
	v_cvt_pk_f16_f32 v11, v80, v81
	s_waitcnt lgkmcnt(8)
	v_pk_mul_f32 v[162:163], v[82:83], v[16:17] op_sel_hi:[1,0]
	v_pk_mul_f32 v[164:165], v[84:85], v[16:17] op_sel_hi:[1,0]
	v_pk_mul_f32 v[166:167], v[86:87], v[16:17] op_sel_hi:[1,0]
	v_pk_mul_f32 v[168:169], v[88:89], v[16:17] op_sel_hi:[1,0]
	v_pk_mul_f32 v[170:171], v[90:91], v[16:17] op_sel_hi:[1,0]
	v_pk_mul_f32 v[172:173], v[92:93], v[16:17] op_sel_hi:[1,0]
	v_pk_mul_f32 v[174:175], v[94:95], v[16:17] op_sel_hi:[1,0]
	v_pk_mul_f32 v[176:177], v[96:97], v[16:17] op_sel_hi:[1,0]
	ds_read_b128 v[130:133], v246 offset:2048
	ds_read_b128 v[134:137], v246 offset:10240
	ds_read_b128 v[138:141], v246 offset:3072
	ds_read_b128 v[142:145], v246 offset:11264
	s_waitcnt lgkmcnt(4)
	v_mfma_f32_32x32x16_f16 v[162:177], v[114:117], v[4:7], v[162:177]
	v_pk_mul_f32 v[146:147], v[98:99], v[16:17] op_sel_hi:[1,0]
	v_pk_mul_f32 v[148:149], v[100:101], v[16:17] op_sel_hi:[1,0]
	v_pk_mul_f32 v[150:151], v[102:103], v[16:17] op_sel_hi:[1,0]
	v_pk_mul_f32 v[152:153], v[104:105], v[16:17] op_sel_hi:[1,0]
	v_pk_mul_f32 v[154:155], v[106:107], v[16:17] op_sel_hi:[1,0]
	v_pk_mul_f32 v[156:157], v[108:109], v[16:17] op_sel_hi:[1,0]
	v_pk_mul_f32 v[158:159], v[110:111], v[16:17] op_sel_hi:[1,0]
	v_pk_mul_f32 v[160:161], v[112:113], v[16:17] op_sel_hi:[1,0]
	s_nop 1
	v_mfma_f32_32x32x16_f16 v[146:161], v[118:121], v[4:7], v[146:161]
	v_cvt_pk_f16_f32 v12, v50, v51
	v_cvt_pk_f16_f32 v13, v52, v53
	v_cvt_pk_f16_f32 v14, v54, v55
	v_cvt_pk_f16_f32 v15, v56, v57
	v_mfma_f32_32x32x16_f16 v[162:177], v[122:125], v[8:11], v[162:177]
	v_cvt_pk_f16_f32 v252, v58, v59
	v_cvt_pk_f16_f32 v253, v60, v61
	v_cvt_pk_f16_f32 v254, v62, v63
	v_cvt_pk_f16_f32 v255, v64, v65
	v_mfma_f32_32x32x16_f16 v[146:161], v[126:129], v[8:11], v[146:161]
	ds_read_b128 v[82:85], v246 offset:4096
	ds_read_b128 v[86:89], v246 offset:12288
	ds_read_b128 v[90:93], v246 offset:5120
	ds_read_b128 v[94:97], v246 offset:13312
	s_waitcnt lgkmcnt(4)
	v_mfma_f32_32x32x16_f16 v[162:177], v[130:133], v[12:15], v[162:177]
	v_cvt_pk_f16_f32 v4, v34, v35
	v_cvt_pk_f16_f32 v5, v36, v37
	v_mfma_f32_32x32x16_f16 v[146:161], v[134:137], v[12:15], v[146:161]
	v_cvt_pk_f16_f32 v6, v38, v39
	v_cvt_pk_f16_f32 v7, v40, v41
	v_mfma_f32_32x32x16_f16 v[162:177], v[138:141], v[252:255], v[162:177]
	v_cvt_pk_f16_f32 v8, v42, v43
	v_cvt_pk_f16_f32 v9, v44, v45
	v_mfma_f32_32x32x16_f16 v[146:161], v[142:145], v[252:255], v[146:161]
	v_cvt_pk_f16_f32 v10, v46, v47
	v_cvt_pk_f16_f32 v11, v48, v49
	ds_read_b128 v[98:101], v246 offset:6144
	ds_read_b128 v[102:105], v246 offset:14336
	ds_read_b128 v[106:109], v246 offset:7168
	ds_read_b128 v[110:113], v246 offset:15360
	s_waitcnt lgkmcnt(4)
	v_mfma_f32_32x32x16_f16 v[162:177], v[82:85], v[4:7], v[162:177]
	v_cvt_pk_f16_f32 v12, v18, v19
	v_cvt_pk_f16_f32 v13, v20, v21
	v_mfma_f32_32x32x16_f16 v[146:161], v[86:89], v[4:7], v[146:161]
	v_cvt_pk_f16_f32 v14, v22, v23
	v_cvt_pk_f16_f32 v15, v24, v25
	v_mfma_f32_32x32x16_f16 v[162:177], v[90:93], v[8:11], v[162:177]
	v_cvt_pk_f16_f32 v252, v26, v27
	v_cvt_pk_f16_f32 v253, v28, v29
	v_mfma_f32_32x32x16_f16 v[146:161], v[94:97], v[8:11], v[146:161]
	v_cvt_pk_f16_f32 v254, v30, v31
	v_cvt_pk_f16_f32 v255, v32, v33
	ds_read_b128 v[18:21], v246 offset:16384
	ds_read_b128 v[22:25], v246 offset:17408
	ds_read_b128 v[26:29], v246 offset:18432
	ds_read_b128 v[30:33], v246 offset:19456
	s_waitcnt lgkmcnt(4)
	v_mfma_f32_32x32x16_f16 v[162:177], v[98:101], v[12:15], v[162:177]
	v_mfma_f32_32x32x16_f16 v[146:161], v[102:105], v[12:15], v[146:161]
	v_mfma_f32_32x32x16_f16 v[162:177], v[106:109], v[252:255], v[162:177]
	v_mfma_f32_32x32x16_f16 v[146:161], v[110:113], v[252:255], v[146:161]
	ds_read_b128 v[130:133], v247 offset:33024
	ds_read_b128 v[134:137], v247 offset:33040
	ds_read_b128 v[138:141], v247 offset:33056
	ds_read_b128 v[142:145], v247 offset:33072
	ds_read_b128 v[114:117], v247 offset:33088
	ds_read_b128 v[118:121], v247 offset:33104
	ds_read_b128 v[122:125], v247 offset:33120
	ds_read_b128 v[126:129], v247 offset:33136
	s_nop 2
	v_cvt_pk_f16_f32 v4, v162, v163
	v_cvt_pk_f16_f32 v5, v164, v165
	v_cvt_pk_f16_f32 v6, v166, v167
	v_cvt_pk_f16_f32 v7, v168, v169
	v_cvt_pk_f16_f32 v8, v170, v171
	v_cvt_pk_f16_f32 v9, v172, v173
	v_cvt_pk_f16_f32 v10, v174, v175
	v_cvt_pk_f16_f32 v11, v176, v177
	v_cvt_pk_f16_f32 v12, v146, v147
	v_cvt_pk_f16_f32 v13, v148, v149
	v_cvt_pk_f16_f32 v14, v150, v151
	v_cvt_pk_f16_f32 v15, v152, v153
	v_cvt_pk_f16_f32 v252, v154, v155
	v_cvt_pk_f16_f32 v253, v156, v157
	v_cvt_pk_f16_f32 v254, v158, v159
	v_cvt_pk_f16_f32 v255, v160, v161
	s_waitcnt lgkmcnt(4)
	ds_read_b128 v[34:37], v246 offset:20480
	ds_read_b128 v[38:41], v246 offset:21504
	ds_read_b128 v[42:45], v246 offset:22528
	ds_read_b128 v[46:49], v246 offset:23552
	v_mfma_f32_32x32x16_f16 v[130:145], v[18:21], v[4:7], v[130:145]
	v_mfma_f32_32x32x16_f16 v[130:145], v[22:25], v[8:11], v[130:145]
	v_mfma_f32_32x32x16_f16 v[130:145], v[26:29], v[12:15], v[130:145]
	v_mfma_f32_32x32x16_f16 v[130:145], v[30:33], v[252:255], v[130:145]
	ds_read_b128 v[146:149], v247 offset:33536
	ds_read_b128 v[150:153], v247 offset:33552
	ds_read_b128 v[154:157], v247 offset:33568
	ds_read_b128 v[158:161], v247 offset:33584
	s_waitcnt lgkmcnt(4)
	ds_read_b128 v[98:101], v247 offset:33152
	ds_read_b128 v[102:105], v247 offset:33168
	ds_read_b128 v[106:109], v247 offset:33184
	ds_read_b128 v[110:113], v247 offset:33200
	ds_read_b128 v[50:53], v246 offset:24576
	ds_read_b128 v[54:57], v246 offset:25600
	ds_read_b128 v[58:61], v246 offset:26624
	ds_read_b128 v[62:65], v246 offset:27648
	v_mfma_f32_32x32x16_f16 v[114:129], v[34:37], v[4:7], v[114:129]
	v_exp_f32_e32 v130, v130
	v_exp_f32_e32 v131, v131
	v_exp_f32_e32 v132, v132
	v_exp_f32_e32 v133, v133
	v_exp_f32_e32 v134, v134
	v_exp_f32_e32 v135, v135
	v_exp_f32_e32 v136, v136
	v_exp_f32_e32 v137, v137
	v_mfma_f32_32x32x16_f16 v[114:129], v[38:41], v[8:11], v[114:129]
	v_exp_f32_e32 v138, v138
	v_exp_f32_e32 v139, v139
	v_exp_f32_e32 v140, v140
	v_exp_f32_e32 v141, v141
	v_exp_f32_e32 v142, v142
	v_exp_f32_e32 v143, v143
	v_exp_f32_e32 v144, v144
	v_exp_f32_e32 v145, v145
	v_mfma_f32_32x32x16_f16 v[114:129], v[42:45], v[12:15], v[114:129]
	v_pk_add_f32 v[130:131], v[130:131], s[82:83]
	v_pk_add_f32 v[132:133], v[132:133], s[82:83]
	v_pk_add_f32 v[134:135], v[134:135], s[82:83]
	v_pk_add_f32 v[136:137], v[136:137], s[82:83]
	v_pk_add_f32 v[138:139], v[138:139], s[82:83]
	v_pk_add_f32 v[140:141], v[140:141], s[82:83]
	v_pk_add_f32 v[142:143], v[142:143], s[82:83]
	v_pk_add_f32 v[144:145], v[144:145], s[82:83]
	v_mfma_f32_32x32x16_f16 v[114:129], v[46:49], v[252:255], v[114:129]
	v_rcp_f32_e32 v130, v130
	v_rcp_f32_e32 v131, v131
	v_rcp_f32_e32 v132, v132
	v_rcp_f32_e32 v133, v133
	v_rcp_f32_e32 v134, v134
	v_rcp_f32_e32 v135, v135
	v_rcp_f32_e32 v136, v136
	v_rcp_f32_e32 v137, v137
	v_rcp_f32_e32 v138, v138
	v_rcp_f32_e32 v139, v139
	v_rcp_f32_e32 v140, v140
	v_rcp_f32_e32 v141, v141
	v_rcp_f32_e32 v142, v142
	v_rcp_f32_e32 v143, v143
	v_rcp_f32_e32 v144, v144
	v_rcp_f32_e32 v145, v145
	s_waitcnt lgkmcnt(8)
	ds_read_b128 v[162:165], v247 offset:33600
	ds_read_b128 v[166:169], v247 offset:33616
	ds_read_b128 v[170:173], v247 offset:33632
	ds_read_b128 v[174:177], v247 offset:33648
	v_mul_f32_e32 v3, v146, v130
	v_mul_f32_e32 v16, v147, v131
	v_mul_f32_e32 v17, v148, v132
	v_fmac_f32_e32 v3, v149, v133
	v_fmac_f32_e32 v16, v150, v134
	v_fmac_f32_e32 v17, v151, v135
	v_fmac_f32_e32 v3, v152, v136
	v_fmac_f32_e32 v16, v153, v137
	v_fmac_f32_e32 v17, v154, v138
	v_fmac_f32_e32 v3, v155, v139
	v_fmac_f32_e32 v16, v156, v140
	v_fmac_f32_e32 v17, v157, v141
	v_fmac_f32_e32 v3, v158, v142
	v_fmac_f32_e32 v16, v159, v143
	v_fmac_f32_e32 v17, v160, v144
	v_fmac_f32_e32 v3, v161, v145
	s_waitcnt lgkmcnt(4)
	ds_read_b128 v[82:85], v247 offset:33216
	ds_read_b128 v[86:89], v247 offset:33232
	ds_read_b128 v[90:93], v247 offset:33248
	ds_read_b128 v[94:97], v247 offset:33264
	ds_read_b128 v[66:69], v246 offset:28672
	ds_read_b128 v[70:73], v246 offset:29696
	ds_read_b128 v[74:77], v246 offset:30720
	ds_read_b128 v[78:81], v246 offset:31744
	v_mfma_f32_32x32x16_f16 v[98:113], v[50:53], v[4:7], v[98:113]
	v_exp_f32_e32 v114, v114
	v_exp_f32_e32 v115, v115
	v_exp_f32_e32 v116, v116
	v_exp_f32_e32 v117, v117
	v_exp_f32_e32 v118, v118
	v_exp_f32_e32 v119, v119
	v_exp_f32_e32 v120, v120
	v_exp_f32_e32 v121, v121
	v_mfma_f32_32x32x16_f16 v[98:113], v[54:57], v[8:11], v[98:113]
	v_exp_f32_e32 v122, v122
	v_exp_f32_e32 v123, v123
	v_exp_f32_e32 v124, v124
	v_exp_f32_e32 v125, v125
	v_exp_f32_e32 v126, v126
	v_exp_f32_e32 v127, v127
	v_exp_f32_e32 v128, v128
	v_exp_f32_e32 v129, v129
	v_mfma_f32_32x32x16_f16 v[98:113], v[58:61], v[12:15], v[98:113]
	v_pk_add_f32 v[114:115], v[114:115], s[82:83]
	v_pk_add_f32 v[116:117], v[116:117], s[82:83]
	v_pk_add_f32 v[118:119], v[118:119], s[82:83]
	v_pk_add_f32 v[120:121], v[120:121], s[82:83]
	v_pk_add_f32 v[122:123], v[122:123], s[82:83]
	v_pk_add_f32 v[124:125], v[124:125], s[82:83]
	v_pk_add_f32 v[126:127], v[126:127], s[82:83]
	v_pk_add_f32 v[128:129], v[128:129], s[82:83]
	v_mfma_f32_32x32x16_f16 v[98:113], v[62:65], v[252:255], v[98:113]
	v_rcp_f32_e32 v114, v114
	v_rcp_f32_e32 v115, v115
	v_rcp_f32_e32 v116, v116
	v_rcp_f32_e32 v117, v117
	v_rcp_f32_e32 v118, v118
	v_rcp_f32_e32 v119, v119
	v_rcp_f32_e32 v120, v120
	v_rcp_f32_e32 v121, v121
	v_rcp_f32_e32 v122, v122
	v_rcp_f32_e32 v123, v123
	v_rcp_f32_e32 v124, v124
	v_rcp_f32_e32 v125, v125
	v_rcp_f32_e32 v126, v126
	v_rcp_f32_e32 v127, v127
	v_rcp_f32_e32 v128, v128
	v_rcp_f32_e32 v129, v129
	s_waitcnt lgkmcnt(8)
	ds_read_b128 v[18:21], v247 offset:33664
	ds_read_b128 v[22:25], v247 offset:33680
	ds_read_b128 v[26:29], v247 offset:33696
	ds_read_b128 v[30:33], v247 offset:33712
	v_fmac_f32_e32 v3, v162, v114
	v_fmac_f32_e32 v16, v163, v115
	v_fmac_f32_e32 v17, v164, v116
	v_fmac_f32_e32 v3, v165, v117
	v_fmac_f32_e32 v16, v166, v118
	v_fmac_f32_e32 v17, v167, v119
	v_fmac_f32_e32 v3, v168, v120
	v_fmac_f32_e32 v16, v169, v121
	v_fmac_f32_e32 v17, v170, v122
	v_fmac_f32_e32 v3, v171, v123
	v_fmac_f32_e32 v16, v172, v124
	v_fmac_f32_e32 v17, v173, v125
	v_fmac_f32_e32 v3, v174, v126
	v_fmac_f32_e32 v16, v175, v127
	v_fmac_f32_e32 v17, v176, v128
	v_fmac_f32_e32 v3, v177, v129
	s_waitcnt lgkmcnt(4)
	ds_read_b128 v[146:149], v247 offset:33728
	ds_read_b128 v[150:153], v247 offset:33744
	ds_read_b128 v[154:157], v247 offset:33760
	ds_read_b128 v[158:161], v247 offset:33776
	v_mfma_f32_32x32x16_f16 v[82:97], v[66:69], v[4:7], v[82:97]
	v_exp_f32_e32 v98, v98
	v_exp_f32_e32 v99, v99
	v_exp_f32_e32 v100, v100
	v_exp_f32_e32 v101, v101
	v_exp_f32_e32 v102, v102
	v_exp_f32_e32 v103, v103
	v_exp_f32_e32 v104, v104
	v_exp_f32_e32 v105, v105
	v_mfma_f32_32x32x16_f16 v[82:97], v[70:73], v[8:11], v[82:97]
	v_exp_f32_e32 v106, v106
	v_exp_f32_e32 v107, v107
	v_exp_f32_e32 v108, v108
	v_exp_f32_e32 v109, v109
	v_exp_f32_e32 v110, v110
	v_exp_f32_e32 v111, v111
	v_exp_f32_e32 v112, v112
	v_exp_f32_e32 v113, v113
	v_mfma_f32_32x32x16_f16 v[82:97], v[74:77], v[12:15], v[82:97]
	v_pk_add_f32 v[98:99], v[98:99], s[82:83]
	v_pk_add_f32 v[100:101], v[100:101], s[82:83]
	v_pk_add_f32 v[102:103], v[102:103], s[82:83]
	v_pk_add_f32 v[104:105], v[104:105], s[82:83]
	v_pk_add_f32 v[106:107], v[106:107], s[82:83]
	v_pk_add_f32 v[108:109], v[108:109], s[82:83]
	v_pk_add_f32 v[110:111], v[110:111], s[82:83]
	v_pk_add_f32 v[112:113], v[112:113], s[82:83]
	v_mfma_f32_32x32x16_f16 v[82:97], v[78:81], v[252:255], v[82:97]
	v_rcp_f32_e32 v98, v98
	v_rcp_f32_e32 v99, v99
	v_rcp_f32_e32 v100, v100
	v_rcp_f32_e32 v101, v101
	v_rcp_f32_e32 v102, v102
	v_rcp_f32_e32 v103, v103
	v_rcp_f32_e32 v104, v104
	v_rcp_f32_e32 v105, v105
	v_rcp_f32_e32 v106, v106
	v_rcp_f32_e32 v107, v107
	v_rcp_f32_e32 v108, v108
	v_rcp_f32_e32 v109, v109
	v_rcp_f32_e32 v110, v110
	v_rcp_f32_e32 v111, v111
	v_rcp_f32_e32 v112, v112
	v_rcp_f32_e32 v113, v113
	s_waitcnt lgkmcnt(4)
	v_fmac_f32_e32 v3, v18, v98
	v_fmac_f32_e32 v16, v19, v99
	v_fmac_f32_e32 v17, v20, v100
	v_fmac_f32_e32 v3, v21, v101
	v_fmac_f32_e32 v16, v22, v102
	v_fmac_f32_e32 v17, v23, v103
	v_fmac_f32_e32 v3, v24, v104
	v_fmac_f32_e32 v16, v25, v105
	v_fmac_f32_e32 v17, v26, v106
	v_fmac_f32_e32 v3, v27, v107
	v_fmac_f32_e32 v16, v28, v108
	v_fmac_f32_e32 v17, v29, v109
	v_fmac_f32_e32 v3, v30, v110
	v_fmac_f32_e32 v16, v31, v111
	v_fmac_f32_e32 v17, v32, v112
	v_fmac_f32_e32 v3, v33, v113
	v_exp_f32_e32 v82, v82
	v_exp_f32_e32 v83, v83
	v_exp_f32_e32 v84, v84
	v_exp_f32_e32 v85, v85
	v_exp_f32_e32 v86, v86
	v_exp_f32_e32 v87, v87
	v_exp_f32_e32 v88, v88
	v_exp_f32_e32 v89, v89
	v_exp_f32_e32 v90, v90
	v_exp_f32_e32 v91, v91
	v_exp_f32_e32 v92, v92
	v_exp_f32_e32 v93, v93
	v_exp_f32_e32 v94, v94
	v_exp_f32_e32 v95, v95
	v_exp_f32_e32 v96, v96
	v_exp_f32_e32 v97, v97
	v_pk_add_f32 v[82:83], v[82:83], s[82:83]
	v_pk_add_f32 v[84:85], v[84:85], s[82:83]
	v_pk_add_f32 v[86:87], v[86:87], s[82:83]
	v_pk_add_f32 v[88:89], v[88:89], s[82:83]
	v_pk_add_f32 v[90:91], v[90:91], s[82:83]
	v_pk_add_f32 v[92:93], v[92:93], s[82:83]
	v_pk_add_f32 v[94:95], v[94:95], s[82:83]
	v_pk_add_f32 v[96:97], v[96:97], s[82:83]
	v_rcp_f32_e32 v82, v82
	v_rcp_f32_e32 v83, v83
	v_rcp_f32_e32 v84, v84
	v_rcp_f32_e32 v85, v85
	v_rcp_f32_e32 v86, v86
	v_rcp_f32_e32 v87, v87
	v_rcp_f32_e32 v88, v88
	v_rcp_f32_e32 v89, v89
	v_rcp_f32_e32 v90, v90
	v_rcp_f32_e32 v91, v91
	v_rcp_f32_e32 v92, v92
	v_rcp_f32_e32 v93, v93
	v_rcp_f32_e32 v94, v94
	v_rcp_f32_e32 v95, v95
	v_rcp_f32_e32 v96, v96
	v_rcp_f32_e32 v97, v97
	s_waitcnt lgkmcnt(0)
	v_fmac_f32_e32 v3, v146, v82
	v_fmac_f32_e32 v16, v147, v83
	v_fmac_f32_e32 v17, v148, v84
	v_fmac_f32_e32 v3, v149, v85
	v_fmac_f32_e32 v16, v150, v86
	v_fmac_f32_e32 v17, v151, v87
	v_fmac_f32_e32 v3, v152, v88
	v_fmac_f32_e32 v16, v153, v89
	v_fmac_f32_e32 v17, v154, v90
	v_fmac_f32_e32 v3, v155, v91
	v_fmac_f32_e32 v16, v156, v92
	v_fmac_f32_e32 v17, v157, v93
	v_fmac_f32_e32 v3, v158, v94
	v_fmac_f32_e32 v16, v159, v95
	v_fmac_f32_e32 v17, v160, v96
	v_fmac_f32_e32 v3, v161, v97
	v_add_f32_e32 v3, v3, v16
	v_add_f32_e32 v3, v3, v17
	v_mov_b32_e32 v4, v3
	s_nop 1
	v_permlane32_swap_b32_e32 v4, v3
	s_and_saveexec_b64 s[8:9], s[10:11]
	s_cbranch_execz .LBB1_156
	s_waitcnt vmcnt(0)
	v_mul_f32_e32 v5, 0x40549a78, v238
	v_exp_f32_e32 v5, v5
	v_add_f32_e32 v3, v3, v4
	v_ashrrev_i32_e32 v7, 31, v235
	v_mov_b32_e32 v6, v235
	v_add_f32_e32 v3, v239, v3
	v_lshl_add_u64 v[6:7], v[6:7], 2, s[52:53]
	v_mul_f32_e32 v3, v5, v3
	global_store_dword v[6:7], v3, off
.LBB1_156:
	s_or_b64 exec, exec, s[8:9]
	s_add_u32 s84, s84, 1
	v_add_u32_e32 v82, 1, v251
	s_cmp_eq_u32 s84, s85
	s_cbranch_scc1 .LBB1_159
	s_waitcnt lgkmcnt(0)
	v_add_u32_e32 v17, 32, v235
	v_cmp_gt_i32_e32 vcc, s17, v235
	v_mov_b32_e32 v238, 0
	v_readlane_b32 s20, v231, 31
	v_sub_u32_e32 v16, v231, v230
	s_and_saveexec_b64 s[10:11], vcc
	s_cbranch_execz .LBB1_146
	v_ashrrev_i32_e32 v5, 31, v17
	v_mov_b32_e32 v4, v17
	v_lshl_add_u64 v[4:5], v[4:5], 2, s[50:51]
	global_load_dword v238, v[4:5], off
	s_branch .LBB1_146
